# speedup vs baseline: 1.0274x; 1.0274x over previous
.LBB2_20:
	s_cmp_gt_i32 s2, 5
	s_cbranch_scc0 .LBB2_49
	s_cmp_gt_i32 s2, 6
	s_cbranch_scc0 .LBB2_51
	v_cmp_gt_u32_e64 s[0:1], 10, v0
	v_mov_b32_e32 v8, 0
	v_mov_b32_e32 v9, 0
	s_movk_i32 s3, 0x64
	v_cmp_gt_u32_e64 s[4:5], s3, v0
	s_movk_i32 s6, 0x100
	v_cmp_gt_u32_e32 vcc, s6, v0
	v_cndmask_b32_e64 v68, 0, v0, s[4:5]
	v_lshlrev_b32_e32 v68, 2, v68
	s_waitcnt lgkmcnt(0)
	s_load_dwordx8 s[40:47], s[16:17], 0x0
	s_load_dwordx2 s[48:49], s[16:17], 0x20
	global_load_dword v66, v68, s[8:9]
	global_load_dword v67, v68, s[10:11]
	s_and_saveexec_b64 s[6:7], vcc
	s_cbranch_execz .Lh_nocs
	v_lshlrev_b32_e32 v69, 2, v0
	global_load_dword v56, v69, s[20:21] nt
	global_load_dword v57, v69, s[20:21] offset:1024 nt
	global_load_dword v58, v69, s[20:21] offset:2048 nt
	global_load_dword v59, v69, s[20:21] offset:3072 nt
	v_add_u32_e32 v68, 0x1000, v69
	global_load_dword v60, v68, s[20:21] nt
	global_load_dword v61, v68, s[20:21] offset:1024 nt
	global_load_dword v62, v68, s[20:21] offset:2048 nt
	global_load_dword v63, v68, s[20:21] offset:3072 nt
	v_add_u32_e32 v68, 0x2000, v69
	global_load_dword v64, v68, s[20:21] nt
	global_load_dword v65, v68, s[20:21] offset:1024 nt
.Lh_nocs:
	s_mov_b64 exec, s[6:7]
	s_and_saveexec_b64 s[4:5], s[0:1]
	s_cbranch_execz .LBB2_30
	v_lshlrev_b32_e32 v21, 2, v0
	v_lshlrev_b32_e32 v18, 8, v0
	global_load_dword v20, v21, s[16:17]
	global_load_dwordx3 v[14:16], v18, s[22:23] offset:52 nt
	global_load_dwordx4 v[2:5], v18, s[22:23] offset:36 nt
	global_load_dwordx4 v[6:9], v18, s[22:23] offset:20 nt
	global_load_dwordx4 v[10:13], v18, s[22:23] offset:4 nt
	global_load_dword v19, v18, s[22:23] nt
	global_load_dword v8, v21, s[12:13]
	s_waitcnt vmcnt(0)
	v_add_u32_e32 v22, 0x7f, v20
	v_ashrrev_i32_e32 v22, 7, v22
	v_cmp_lt_i32_e32 vcc, 0, v22
	v_add_f32_e32 v19, 0, v19
	s_nop 0
	v_cndmask_b32_e32 v19, 0, v19, vcc
	v_cmp_lt_i32_e32 vcc, 1, v22
	s_nop 0
	v_cndmask_b32_e32 v10, 0, v10, vcc
	v_cmp_lt_i32_e32 vcc, 2, v22
	v_add_f32_e32 v10, v19, v10
	s_nop 0
	v_cndmask_b32_e32 v11, 0, v11, vcc
	v_cmp_lt_i32_e32 vcc, 3, v22
	v_add_f32_e32 v10, v10, v11
	s_nop 0
	v_cndmask_b32_e32 v11, 0, v12, vcc
	v_cmp_lt_i32_e32 vcc, 4, v22
	v_add_f32_e32 v10, v10, v11
	s_nop 0
	v_cndmask_b32_e32 v11, 0, v13, vcc
	v_cmp_lt_i32_e32 vcc, 5, v22
	v_add_f32_e32 v10, v10, v11
	s_nop 0
	v_cndmask_b32_e32 v6, 0, v6, vcc
	v_cmp_lt_i32_e32 vcc, 6, v22
	v_add_f32_e32 v6, v10, v6
	s_nop 0
	v_cndmask_b32_e32 v7, 0, v7, vcc
	v_cmp_lt_i32_e32 vcc, 7, v22
	v_add_f32_e32 v6, v6, v7
	s_nop 0
	v_cndmask_b32_e32 v7, 0, v8, vcc
	v_cmp_lt_i32_e32 vcc, 8, v22
	v_add_f32_e32 v6, v6, v7
	s_nop 0
	v_cndmask_b32_e32 v7, 0, v9, vcc
	v_cmp_lt_i32_e32 vcc, 9, v22
	v_add_f32_e32 v6, v6, v7
	s_nop 0
	v_cndmask_b32_e32 v2, 0, v2, vcc
	v_cmp_lt_i32_e32 vcc, 10, v22
	v_add_f32_e32 v2, v6, v2
	s_nop 0
	v_cndmask_b32_e32 v3, 0, v3, vcc
	v_cmp_lt_i32_e32 vcc, 11, v22
	v_add_f32_e32 v2, v2, v3
	s_nop 0
	v_cndmask_b32_e32 v3, 0, v4, vcc
	v_cmp_lt_i32_e32 vcc, 12, v22
	v_add_f32_e32 v2, v2, v3
	s_nop 0
	v_cndmask_b32_e32 v3, 0, v5, vcc
	v_cmp_lt_i32_e32 vcc, 13, v22
	v_add_f32_e32 v2, v2, v3
	s_nop 0
	v_cndmask_b32_e32 v3, 0, v14, vcc
	v_cmp_lt_i32_e32 vcc, 14, v22
	v_add_f32_e32 v2, v2, v3
	s_nop 0
	v_cndmask_b32_e32 v3, 0, v15, vcc
	v_cmp_lt_i32_e32 vcc, 15, v22
	v_add_f32_e32 v2, v2, v3
	s_nop 0
	v_cndmask_b32_e32 v3, 0, v16, vcc
	v_add_f32_e32 v4, v2, v3
	v_cmp_lt_i32_e32 vcc, 16, v22
	s_and_saveexec_b64 s[6:7], vcc
	s_cbranch_execz .LBB2_29
	v_mov_b32_e32 v19, 0
	v_lshl_add_u64 v[2:3], s[22:23], 0, v[18:19]
	v_lshl_add_u64 v[2:3], v[2:3], 0, 64
	v_add_u32_e32 v5, -16, v22
	s_mov_b64 s[22:23], 0

.LBB2_29:
	s_or_b64 exec, exec, s[6:7]
	v_cvt_f32_i32_e32 v2, v20
	v_div_scale_f32 v3, s[6:7], v2, v2, v4
	v_rcp_f32_e32 v5, v3
	s_nop 0
	v_fma_f32 v6, -v3, v5, 1.0
	v_fmac_f32_e32 v5, v6, v5
	v_div_scale_f32 v6, vcc, v4, v2, v4
	v_mul_f32_e32 v7, v6, v5
	v_fma_f32 v9, -v3, v7, v6
	v_fmac_f32_e32 v7, v9, v5
	v_fma_f32 v3, -v3, v7, v6
	v_div_fmas_f32 v3, v3, v5, v7
	v_div_fixup_f32 v9, v3, v2, v4
.LBB2_30:
	s_or_b64 exec, exec, s[4:5]
	s_movk_i32 s3, 0x64
	v_cmp_gt_u32_e64 s[4:5], s3, v0
	s_movk_i32 s6, 0x100
	v_cmp_gt_u32_e32 vcc, s6, v0
	v_cndmask_b32_e64 v4, 0, v0, s[4:5]
	v_lshlrev_b32_e32 v2, 2, v4
	s_waitcnt vmcnt(0) lgkmcnt(0)
	v_mov_b32_e32 v6, v66
	v_mov_b32_e32 v7, v67
	s_and_saveexec_b64 s[34:35], vcc
	s_cbranch_execz .LBB2_32
	v_lshlrev_b32_e32 v2, 2, v0
	s_mov_b64 s[20:21], s[40:41]
	s_mov_b64 s[22:23], s[42:43]
	s_mov_b64 s[24:25], s[44:45]
	s_mov_b64 s[26:27], s[46:47]
	s_mov_b64 s[36:37], s[48:49]
	v_mov_b32_e32 v5, v56
	v_mov_b32_e32 v14, v57
	v_mov_b32_e32 v15, v58
	v_mov_b32_e32 v16, v59
	v_mov_b32_e32 v3, v60
	v_mov_b32_e32 v18, v61
	v_mov_b32_e32 v19, v62
	v_mov_b32_e32 v20, v63
	v_mov_b32_e32 v21, v64
	v_mov_b32_e32 v22, v65
	v_cvt_f32_i32_e32 v10, s20
	v_cvt_f32_i32_e32 v11, s21
	v_cvt_f32_i32_e32 v12, s22
	v_cvt_f32_i32_e32 v13, s23
	v_cvt_f32_i32_e32 v23, s24
	s_waitcnt vmcnt(9)
	v_div_scale_f32 v24, s[6:7], v10, v10, v5
	s_waitcnt vmcnt(8)
	v_div_scale_f32 v26, s[6:7], v11, v11, v14
	v_rcp_f32_e32 v32, v24
	s_waitcnt vmcnt(7)
	v_div_scale_f32 v28, s[8:9], v12, v12, v15
	v_rcp_f32_e32 v33, v26
	v_rcp_f32_e32 v34, v28
	v_fma_f32 v39, -v24, v32, 1.0
	v_div_scale_f32 v25, vcc, v5, v10, v5
	s_waitcnt vmcnt(6)
	v_div_scale_f32 v30, s[10:11], v13, v13, v16
	v_fma_f32 v40, -v26, v33, 1.0
	v_fmac_f32_e32 v32, v39, v32
	v_div_scale_f32 v27, s[6:7], v14, v11, v14
	v_rcp_f32_e32 v35, v30
	v_fma_f32 v41, -v28, v34, 1.0
	v_fmac_f32_e32 v33, v40, v33
	v_mul_f32_e32 v39, v25, v32
	v_div_scale_f32 v29, s[8:9], v15, v12, v15
	v_fmac_f32_e32 v34, v41, v34
	v_mul_f32_e32 v40, v27, v33
	v_fma_f32 v43, -v24, v39, v25
	v_mul_f32_e32 v41, v29, v34
	v_fma_f32 v44, -v26, v40, v27
	v_fmac_f32_e32 v39, v43, v32
	v_fma_f32 v45, -v28, v41, v29
	v_fmac_f32_e32 v40, v44, v33
	v_fma_f32 v24, -v24, v39, v25
	s_waitcnt vmcnt(5)
	v_div_scale_f32 v36, s[12:13], v23, v23, v3
	v_fma_f32 v42, -v30, v35, 1.0
	v_fmac_f32_e32 v41, v45, v34
	v_fma_f32 v25, -v26, v40, v27
	v_div_fmas_f32 v24, v24, v32, v39
	s_mov_b64 vcc, s[6:7]
	v_div_scale_f32 v31, s[10:11], v16, v13, v16
	v_rcp_f32_e32 v38, v36
	v_fmac_f32_e32 v35, v42, v35
	v_fma_f32 v26, -v28, v41, v29
	v_div_fixup_f32 v5, v24, v10, v5
	v_div_fmas_f32 v10, v25, v33, v40
	s_mov_b64 vcc, s[8:9]
	v_mul_f32_e32 v42, v31, v35
	v_div_fixup_f32 v10, v10, v11, v14
	v_div_fmas_f32 v11, v26, v34, v41
	v_fma_f32 v46, -v30, v42, v31
	v_div_fixup_f32 v11, v11, v12, v15
	v_cvt_f32_i32_e32 v15, s25
	v_fmac_f32_e32 v42, v46, v35
	v_fma_f32 v47, -v36, v38, 1.0
	v_fma_f32 v27, -v30, v42, v31
	v_add_f32_e32 v24, 0, v5
	s_mov_b64 vcc, s[10:11]
	v_div_scale_f32 v37, s[12:13], v3, v23, v3
	v_fmac_f32_e32 v38, v47, v38
	v_add_f32_e32 v14, v24, v10
	v_div_fmas_f32 v12, v27, v35, v42
	v_mul_f32_e32 v28, v37, v38
	v_add_f32_e32 v14, v14, v11
	v_div_fixup_f32 v12, v12, v13, v16
	s_waitcnt vmcnt(4)
	v_div_scale_f32 v16, s[6:7], v15, v15, v18
	v_add_f32_e32 v13, v14, v12
	v_fma_f32 v14, -v36, v28, v37
	v_rcp_f32_e32 v24, v16
	v_fmac_f32_e32 v28, v14, v38
	v_fma_f32 v14, -v36, v28, v37
	s_mov_b64 vcc, s[12:13]
	v_div_fmas_f32 v14, v14, v38, v28
	v_div_fixup_f32 v3, v14, v23, v3
	v_fma_f32 v14, -v16, v24, 1.0
	v_fmac_f32_e32 v24, v14, v24
	v_div_scale_f32 v14, vcc, v18, v15, v18
	v_cvt_f32_i32_e32 v26, s26
	v_mul_f32_e32 v23, v14, v24
	v_fma_f32 v25, -v16, v23, v14
	v_fmac_f32_e32 v23, v25, v24
	v_fma_f32 v14, -v16, v23, v14
	s_waitcnt vmcnt(3)
	v_div_scale_f32 v16, s[6:7], v26, v26, v19
	v_rcp_f32_e32 v25, v16
	v_div_fmas_f32 v14, v14, v24, v23
	v_div_fixup_f32 v14, v14, v15, v18
	v_cvt_f32_i32_e32 v24, s27
	v_fma_f32 v15, -v16, v25, 1.0
	v_fmac_f32_e32 v25, v15, v25
	v_div_scale_f32 v15, vcc, v19, v26, v19
	v_mul_f32_e32 v18, v15, v25
	v_fma_f32 v23, -v16, v18, v15
	v_fmac_f32_e32 v18, v23, v25
	v_fma_f32 v15, -v16, v18, v15
	s_waitcnt vmcnt(2)
	v_div_scale_f32 v16, s[6:7], v24, v24, v20
	v_rcp_f32_e32 v23, v16
	v_div_fmas_f32 v15, v15, v25, v18
	v_div_fixup_f32 v15, v15, v26, v19
	v_cvt_f32_i32_e32 v26, s36
	v_fma_f32 v18, -v16, v23, 1.0
	v_fmac_f32_e32 v23, v18, v23
	v_div_scale_f32 v18, vcc, v20, v24, v20
	v_mul_f32_e32 v19, v18, v23
	v_fma_f32 v25, -v16, v19, v18
	v_fmac_f32_e32 v19, v25, v23
	v_fma_f32 v16, -v16, v19, v18
	s_waitcnt vmcnt(1)
	v_div_scale_f32 v18, s[6:7], v26, v26, v21
	v_rcp_f32_e32 v25, v18
	v_div_fmas_f32 v16, v16, v23, v19
	v_div_fixup_f32 v16, v16, v24, v20
	v_cvt_f32_i32_e32 v24, s37
	v_fma_f32 v19, -v18, v25, 1.0
	v_fmac_f32_e32 v25, v19, v25
	v_div_scale_f32 v19, vcc, v21, v26, v21
	v_mul_f32_e32 v20, v19, v25
	v_fma_f32 v23, -v18, v20, v19
	v_fmac_f32_e32 v20, v23, v25
	v_fma_f32 v18, -v18, v20, v19
	s_waitcnt vmcnt(0)
	v_div_scale_f32 v19, s[6:7], v24, v24, v22
	v_rcp_f32_e32 v23, v19
	v_div_fmas_f32 v18, v18, v25, v20
	v_div_fixup_f32 v18, v18, v26, v21
	v_add_f32_e32 v13, v13, v3
	v_fma_f32 v20, -v19, v23, 1.0
	v_fmac_f32_e32 v23, v20, v23
	v_div_scale_f32 v20, vcc, v22, v24, v22
	v_mul_f32_e32 v21, v20, v23
	v_fma_f32 v25, -v19, v21, v20
	v_add_f32_e32 v13, v13, v14
	v_fmac_f32_e32 v21, v25, v23
	v_add_f32_e32 v13, v13, v15
	v_fma_f32 v19, -v19, v21, v20
	v_add_f32_e32 v13, v13, v16
	v_div_fmas_f32 v19, v19, v23, v21
	v_add_f32_e32 v13, v13, v18
	v_div_fixup_f32 v19, v19, v24, v22
	v_add_f32_e32 v13, v13, v19
	s_mov_b32 s8, 0x41200000
	v_div_scale_f32 v20, s[6:7], s8, s8, v13
	v_rcp_f32_e32 v21, v20
	ds_write_b32 v2, v5
	v_fma_f32 v22, -v20, v21, 1.0
	v_fmac_f32_e32 v21, v22, v21
	v_div_scale_f32 v22, vcc, v13, s8, v13
	v_mul_f32_e32 v23, v22, v21
	v_fma_f32 v24, -v20, v23, v22
	v_fmac_f32_e32 v23, v24, v21
	v_fma_f32 v20, -v20, v23, v22
	v_div_fmas_f32 v20, v20, v21, v23
	v_div_fixup_f32 v13, v20, s8, v13
	v_sub_f32_e32 v5, v5, v13
	ds_write_b32 v2, v5 offset:10400
	ds_write_b32 v2, v10 offset:1040
	v_sub_f32_e32 v5, v10, v13
	ds_write_b32 v2, v5 offset:11440
	ds_write_b32 v2, v11 offset:2080
	v_sub_f32_e32 v5, v11, v13
	ds_write_b32 v2, v5 offset:12480
	ds_write_b32 v2, v12 offset:3120
	v_sub_f32_e32 v5, v12, v13
	ds_write_b32 v2, v5 offset:13520
	ds_write_b32 v2, v3 offset:4160
	v_sub_f32_e32 v3, v3, v13
	ds_write_b32 v2, v3 offset:14560
	ds_write_b32 v2, v14 offset:5200
	v_sub_f32_e32 v3, v14, v13
	ds_write_b32 v2, v3 offset:15600
	ds_write_b32 v2, v15 offset:6240
	v_sub_f32_e32 v3, v15, v13
	ds_write_b32 v2, v3 offset:16640
	ds_write_b32 v2, v16 offset:7280
	v_sub_f32_e32 v3, v16, v13
	ds_write_b32 v2, v3 offset:17680
	ds_write_b32 v2, v18 offset:8320
	v_sub_f32_e32 v3, v18, v13
	ds_write_b32 v2, v3 offset:18720
	ds_write_b32 v2, v19 offset:9360
	v_sub_f32_e32 v3, v19, v13
	ds_write_b32 v2, v3 offset:19760

.LBB2_70:
	s_and_b64 vcc, exec, s[30:31]
	s_cbranch_vccz .LBB2_112
	v_cmp_gt_u32_e64 s[0:1], 10, v0
	s_mov_b32 s25, 0
	s_nop 0
	v_cndmask_b32_e64 v2, 0, v0, s[0:1]
	v_mad_u64_u32 v[2:3], s[2:3], s24, 10, v[2:3]
	v_mov_b32_e32 v3, 0
	s_waitcnt lgkmcnt(0)
	v_lshl_add_u64 v[4:5], v[2:3], 2, s[14:15]
	global_load_dword v6, v[4:5], off
	s_lshl_b64 s[2:3], s[24:25], 2
	s_add_u32 s2, s16, s2
	s_addc_u32 s3, s17, s3
	s_load_dword s14, s[2:3], 0x0
	v_mov_b32_e32 v25, v3
	v_mov_b32_e32 v24, v3
	v_mov_b32_e32 v23, v3
	v_mov_b32_e32 v22, v3
	s_waitcnt lgkmcnt(0)
	s_add_i32 s2, s14, 0x7f
	s_and_b32 s15, s2, 0xffffff80
	v_cmp_gt_i32_e32 vcc, s15, v0
	v_mov_b32_e32 v21, v3
	v_mov_b32_e32 v20, v3
	v_mov_b32_e32 v19, v3
	v_mov_b32_e32 v18, v3
	v_mov_b32_e32 v2, v3
	s_and_saveexec_b64 s[6:7], vcc
	s_cbranch_execz .LBB2_85
	s_mul_i32 s2, s24, 0x30000
	s_add_u32 s2, s18, s2
	s_addc_u32 s3, s19, 0
	v_lshlrev_b32_e32 v4, 2, v0
	s_cmpk_gt_i32 s14, 0x360
	s_cselect_b64 s[8:9], -1, 0
	s_cmpk_lt_i32 s14, 0x361
	v_add_u32_e32 v2, 0x2000, v4
	global_load_dword v20, v2, s[2:3] offset:-4096 nt
	global_load_dword v22, v2, s[2:3] nt
	v_add_u32_e32 v2, 0x4000, v4
	global_load_dword v18, v2, s[2:3] offset:-4096 nt
	global_load_dword v24, v2, s[2:3] nt
	v_add_u32_e32 v2, 0x6000, v4
	global_load_dword v21, v2, s[2:3] offset:-4096 nt
	global_load_dword v23, v2, s[2:3] nt
	v_add_u32_e32 v2, 0x8000, v4
	global_load_dword v19, v2, s[2:3] offset:-4096 nt
	global_load_dword v25, v2, s[2:3] nt
	v_add_u32_e32 v2, 0xa000, v4
	global_load_dword v29, v2, s[2:3] offset:-4096 nt
	v_add_u32_e32 v2, 0xc000, v4
	global_load_dword v5, v2, s[2:3] offset:-4096 nt
	global_load_dword v26, v2, s[2:3] nt
	v_add_u32_e32 v2, 0xe000, v4
	global_load_dword v31, v2, s[2:3] offset:-4096 nt
	global_load_dword v30, v2, s[2:3] nt
	v_add_u32_e32 v2, 0x10000, v4
	global_load_dword v34, v2, s[2:3] offset:-4096 nt
	global_load_dword v28, v2, s[2:3] nt
	v_add_u32_e32 v2, 0x12000, v4
	global_load_dword v35, v2, s[2:3] offset:-4096 nt
	global_load_dword v42, v2, s[2:3] nt
	v_add_u32_e32 v2, 0x14000, v4
	global_load_dword v46, v2, s[2:3] offset:-4096 nt
	global_load_dword v39, v2, s[2:3] nt
	v_add_u32_e32 v2, 0x16000, v4
	global_load_dword v45, v2, s[2:3] offset:-4096 nt
	v_add_u32_e32 v2, 0x18000, v4
	global_load_dword v27, v2, s[2:3] nt
	v_add_u32_e32 v2, 0x1a000, v4
	global_load_dword v33, v2, s[2:3] offset:-4096 nt
	global_load_dword v32, v2, s[2:3] nt
	v_add_u32_e32 v2, 0x1c000, v4
	global_load_dword v36, v2, s[2:3] offset:-4096 nt
	global_load_dword v47, v4, s[2:3] nt
	global_load_dword v37, v2, s[2:3] nt
	v_add_u32_e32 v2, 0x1e000, v4
	global_load_dword v41, v2, s[2:3] offset:-4096 nt
	global_load_dword v40, v2, s[2:3] nt
	v_add_u32_e32 v2, 0x20000, v4
	global_load_dword v44, v2, s[2:3] offset:-4096 nt
	global_load_dword v38, v2, s[2:3] nt
	v_add_u32_e32 v2, 0x22000, v4
	global_load_dword v43, v2, s[2:3] offset:-4096 nt
	s_cbranch_scc1 .LBB2_74
	v_add_u32_e32 v2, 0x24000, v4
	global_load_dword v7, v2, s[2:3]
	v_add_u32_e32 v2, 0x26000, v4
	global_load_dword v8, v2, s[2:3] offset:-4096
	global_load_dword v9, v2, s[2:3]
	v_add_u32_e32 v2, 0x28000, v4
	global_load_dword v10, v2, s[2:3] offset:-4096
	global_load_dword v11, v2, s[2:3]
	v_add_u32_e32 v2, 0x2a000, v4
	global_load_dword v12, v2, s[2:3] offset:-4096
	global_load_dword v13, v2, s[2:3]
	v_add_u32_e32 v2, 0x2c000, v4
	global_load_dword v14, v2, s[2:3] offset:-4096
	global_load_dword v15, v2, s[2:3]
	v_add_u32_e32 v2, 0x2e000, v4
	global_load_dword v16, v2, s[2:3] offset:-4096
.LBB2_74:
	s_waitcnt vmcnt(13)
	v_max_f32_e32 v2, v46, v46
	v_max_f32_e32 v3, v25, v25
	s_waitcnt vmcnt(11)
	v_min_f32_e32 v2, v3, v2
	s_waitcnt vmcnt(6)
	v_max_f32_e32 v3, v47, v47
	v_min_f32_e32 v23, v23, v45
	v_min_f32_e32 v29, v29, v42
	v_min_f32_e32 v19, v19, v39
	v_max_f32_e32 v25, v3, v2
	v_max_f32_e32 v47, v22, v35
	v_max_f32_e32 v45, v23, v31
	v_max_f32_e32 v42, v20, v29
	v_max_f32_e32 v48, v21, v30
	v_max_f32_e32 v49, v18, v28
	v_max_f32_e32 v39, v19, v26
	v_min_f32_e32 v2, v3, v2
	v_min_f32_e32 v3, v24, v34
	v_min_f32_e32 v22, v22, v35
	v_min_f32_e32 v23, v23, v31
	v_min_f32_e32 v20, v20, v29
	v_min_f32_e32 v21, v21, v30
	v_min_f32_e32 v18, v18, v28
	v_min_f32_e32 v19, v19, v26
	v_max_f32_e32 v46, v24, v34
	v_min_f32_e32 v24, v2, v3
	v_min_f32_e32 v29, v20, v21
	v_min_f32_e32 v26, v18, v19
	v_max_f32_e32 v2, v2, v3
	v_max_f32_e32 v3, v22, v23
	v_max_f32_e32 v20, v20, v21
	v_max_f32_e32 v18, v18, v19
	v_min_f32_e32 v31, v22, v23
	v_min_f32_e32 v22, v2, v3
	v_min_f32_e32 v19, v20, v18
	v_min_f32_e32 v21, v22, v19
	v_max_f32_e32 v19, v22, v19
	v_max_f32_e32 v2, v2, v3
	v_max_f32_e32 v3, v20, v18
	v_min_f32_e32 v20, v47, v45
	v_min_f32_e32 v22, v49, v39
	v_min3_f32 v20, v25, v46, v20
	v_min3_f32 v22, v42, v48, v22
	v_min_f32_e32 v34, v24, v31
	v_min_f32_e32 v28, v29, v26
	v_max_f32_e32 v24, v24, v31
	v_max_f32_e32 v26, v29, v26
	v_max_f32_e32 v18, v2, v3
	v_max_f32_e32 v23, v20, v22
	s_waitcnt vmcnt(3)
	v_max_f32_e32 v35, v40, v40
	s_waitcnt vmcnt(1)
	v_min_f32_e32 v30, v34, v28
	v_max_f32_e32 v28, v34, v28
	v_min_f32_e32 v29, v24, v26
	v_max_f32_e32 v24, v24, v26
	v_min3_f32 v20, v20, v22, v44
	v_max_f32_e32 v25, v36, v36
	v_max_f32_e32 v31, v41, v41
	s_waitcnt vmcnt(0)
	v_min3_f32 v2, v2, v3, v43
	v_max_f32_e32 v3, v33, v33
	v_min_f32_e32 v23, v23, v35
	v_min_f32_e32 v18, v18, v38
	v_max_f32_e32 v22, v30, v20
	v_max_f32_e32 v26, v21, v25
	v_max_f32_e32 v33, v2, v3
	v_max_f32_e32 v35, v28, v23
	v_max_f32_e32 v36, v19, v32
	v_max_f32_e32 v39, v24, v37
	v_max_f32_e32 v38, v18, v27
	v_min_f32_e32 v30, v30, v20
	v_min_f32_e32 v21, v21, v25
	v_min_f32_e32 v25, v29, v31
	v_min_f32_e32 v3, v2, v3
	v_min_f32_e32 v28, v28, v23
	v_min_f32_e32 v19, v19, v32
	v_min_f32_e32 v24, v24, v37
	v_min_f32_e32 v27, v18, v27
	v_max_f32_e32 v34, v29, v31
	v_min_f32_e32 v20, v30, v21
	v_min_f32_e32 v2, v25, v3
	v_min_f32_e32 v31, v28, v19
	v_min_f32_e32 v32, v24, v27
	v_max_f32_e32 v21, v30, v21
	v_max_f32_e32 v3, v25, v3
	v_max_f32_e32 v28, v28, v19
	v_max_f32_e32 v27, v24, v27
	v_min_f32_e32 v25, v21, v3
	v_min_f32_e32 v19, v28, v27
	v_min_f32_e32 v24, v25, v19
	v_max_f32_e32 v19, v25, v19
	v_max_f32_e32 v3, v21, v3
	v_max_f32_e32 v25, v28, v27
	v_min_f32_e32 v21, v3, v25
	v_max_f32_e32 v3, v3, v25
	v_min_f32_e32 v25, v34, v33
	v_min_f32_e32 v29, v20, v2
	v_min_f32_e32 v18, v31, v32
	v_min3_f32 v22, v22, v26, v25
	v_min_f32_e32 v25, v39, v38
	v_min_f32_e32 v23, v29, v18
	v_max_f32_e32 v18, v29, v18
	v_max_f32_e32 v2, v20, v2
	v_max_f32_e32 v29, v31, v32
	v_min3_f32 v26, v35, v36, v25
	v_cndmask_b32_e64 v27, 0, 1, s[8:9]
	v_min_f32_e32 v20, v2, v29
	v_max_f32_e32 v2, v2, v29
	v_min_f32_e32 v25, v22, v26
	v_cmp_ne_u32_e64 s[2:3], 1, v27
	s_andn2_b64 vcc, exec, s[8:9]
	v_max_f32_e32 v22, v22, v26
	s_cbranch_vccnz .LBB2_76
	v_max_f32_e32 v26, v14, v14
	v_max_f32_e32 v31, v16, v16
	v_max_f32_e32 v33, v13, v13
	v_max_f32_e32 v38, v15, v15
	v_min_f32_e32 v25, v25, v26
	v_max_f32_e32 v27, v10, v10
	v_max_f32_e32 v29, v12, v12
	v_min_f32_e32 v21, v21, v31
	v_max_f32_e32 v31, v8, v8
	v_min_f32_e32 v22, v22, v33
	v_max_f32_e32 v34, v9, v9
	v_max_f32_e32 v36, v11, v11
	v_min_f32_e32 v3, v3, v38
	v_max_f32_e32 v38, v7, v7
	v_max_f32_e32 v26, v23, v25
	v_max_f32_e32 v28, v24, v27
	v_max_f32_e32 v30, v20, v29
	v_max_f32_e32 v32, v21, v31
	v_max_f32_e32 v33, v18, v22
	v_max_f32_e32 v35, v19, v34
	v_max_f32_e32 v37, v2, v36
	v_max_f32_e32 v39, v3, v38
	v_min_f32_e32 v25, v23, v25
	v_min_f32_e32 v24, v24, v27
	v_min_f32_e32 v29, v20, v29
	v_min_f32_e32 v21, v21, v31
	v_min_f32_e32 v22, v18, v22
	v_min_f32_e32 v19, v19, v34
	v_min_f32_e32 v36, v2, v36
	v_min_f32_e32 v3, v3, v38
	v_min_f32_e32 v27, v25, v24
	v_min_f32_e32 v20, v29, v21
	v_min_f32_e32 v34, v22, v19
	v_min_f32_e32 v2, v36, v3
	v_min_f32_e32 v31, v27, v20
	v_min_f32_e32 v18, v34, v2
	v_max_f32_e32 v27, v27, v20
	v_max_f32_e32 v2, v34, v2
	v_max_f32_e32 v25, v25, v24
	v_max_f32_e32 v21, v29, v21
	v_max_f32_e32 v22, v22, v19
	v_max_f32_e32 v3, v36, v3
	v_min_f32_e32 v20, v27, v2
	v_max_f32_e32 v2, v27, v2
	v_min_f32_e32 v27, v25, v21
	v_min_f32_e32 v19, v22, v3
	v_max_f32_e32 v25, v25, v21
	v_max_f32_e32 v3, v22, v3
	v_min_f32_e32 v21, v25, v3
	v_max_f32_e32 v3, v25, v3
	v_min_f32_e32 v22, v30, v32
	v_min_f32_e32 v25, v37, v39
	v_min3_f32 v22, v26, v28, v22
	v_min3_f32 v26, v33, v35, v25
	v_min_f32_e32 v23, v31, v18
	v_max_f32_e32 v18, v31, v18
	v_min_f32_e32 v24, v27, v19
	v_max_f32_e32 v19, v27, v19
	v_min_f32_e32 v25, v22, v26
	v_max_f32_e32 v22, v22, v26

.LBB2_85:
	s_or_b64 exec, exec, s[6:7]
	v_mov_b32_e32 v1, 0x7140
	v_mad_u32_u24 v1, v17, 48, v1
	v_add_f32_dpp v3, v3, v3 quad_perm:[1,0,3,2] row_mask:0xf bank_mask:0xf bound_ctrl:1
	v_add_f32_dpp v25, v25, v25 quad_perm:[1,0,3,2] row_mask:0xf bank_mask:0xf bound_ctrl:1
	v_add_f32_dpp v24, v24, v24 quad_perm:[1,0,3,2] row_mask:0xf bank_mask:0xf bound_ctrl:1
	v_add_f32_dpp v23, v23, v23 quad_perm:[1,0,3,2] row_mask:0xf bank_mask:0xf bound_ctrl:1
	v_add_f32_dpp v22, v22, v22 quad_perm:[1,0,3,2] row_mask:0xf bank_mask:0xf bound_ctrl:1
	v_add_f32_dpp v21, v21, v21 quad_perm:[1,0,3,2] row_mask:0xf bank_mask:0xf bound_ctrl:1
	v_add_f32_dpp v20, v20, v20 quad_perm:[1,0,3,2] row_mask:0xf bank_mask:0xf bound_ctrl:1
	v_add_f32_dpp v19, v19, v19 quad_perm:[1,0,3,2] row_mask:0xf bank_mask:0xf bound_ctrl:1
	v_add_f32_dpp v18, v18, v18 quad_perm:[1,0,3,2] row_mask:0xf bank_mask:0xf bound_ctrl:1
	v_add_f32_dpp v2, v2, v2 quad_perm:[1,0,3,2] row_mask:0xf bank_mask:0xf bound_ctrl:1
	v_add_f32_dpp v3, v3, v3 quad_perm:[2,3,0,1] row_mask:0xf bank_mask:0xf bound_ctrl:1
	v_add_f32_dpp v25, v25, v25 quad_perm:[2,3,0,1] row_mask:0xf bank_mask:0xf bound_ctrl:1
	v_add_f32_dpp v24, v24, v24 quad_perm:[2,3,0,1] row_mask:0xf bank_mask:0xf bound_ctrl:1
	v_add_f32_dpp v23, v23, v23 quad_perm:[2,3,0,1] row_mask:0xf bank_mask:0xf bound_ctrl:1
	v_add_f32_dpp v22, v22, v22 quad_perm:[2,3,0,1] row_mask:0xf bank_mask:0xf bound_ctrl:1
	v_add_f32_dpp v21, v21, v21 quad_perm:[2,3,0,1] row_mask:0xf bank_mask:0xf bound_ctrl:1
	v_add_f32_dpp v20, v20, v20 quad_perm:[2,3,0,1] row_mask:0xf bank_mask:0xf bound_ctrl:1
	v_add_f32_dpp v19, v19, v19 quad_perm:[2,3,0,1] row_mask:0xf bank_mask:0xf bound_ctrl:1
	v_add_f32_dpp v18, v18, v18 quad_perm:[2,3,0,1] row_mask:0xf bank_mask:0xf bound_ctrl:1
	v_add_f32_dpp v2, v2, v2 quad_perm:[2,3,0,1] row_mask:0xf bank_mask:0xf bound_ctrl:1
	v_add_f32_dpp v3, v3, v3 row_half_mirror row_mask:0xf bank_mask:0xf bound_ctrl:1
	v_add_f32_dpp v25, v25, v25 row_half_mirror row_mask:0xf bank_mask:0xf bound_ctrl:1
	v_add_f32_dpp v24, v24, v24 row_half_mirror row_mask:0xf bank_mask:0xf bound_ctrl:1
	v_add_f32_dpp v23, v23, v23 row_half_mirror row_mask:0xf bank_mask:0xf bound_ctrl:1
	v_add_f32_dpp v22, v22, v22 row_half_mirror row_mask:0xf bank_mask:0xf bound_ctrl:1
	v_add_f32_dpp v21, v21, v21 row_half_mirror row_mask:0xf bank_mask:0xf bound_ctrl:1
	v_add_f32_dpp v20, v20, v20 row_half_mirror row_mask:0xf bank_mask:0xf bound_ctrl:1
	v_add_f32_dpp v19, v19, v19 row_half_mirror row_mask:0xf bank_mask:0xf bound_ctrl:1
	v_add_f32_dpp v18, v18, v18 row_half_mirror row_mask:0xf bank_mask:0xf bound_ctrl:1
	v_add_f32_dpp v2, v2, v2 row_half_mirror row_mask:0xf bank_mask:0xf bound_ctrl:1
	v_add_f32_dpp v3, v3, v3 row_mirror row_mask:0xf bank_mask:0xf bound_ctrl:1
	v_add_f32_dpp v25, v25, v25 row_mirror row_mask:0xf bank_mask:0xf bound_ctrl:1
	v_add_f32_dpp v24, v24, v24 row_mirror row_mask:0xf bank_mask:0xf bound_ctrl:1
	v_add_f32_dpp v23, v23, v23 row_mirror row_mask:0xf bank_mask:0xf bound_ctrl:1
	v_add_f32_dpp v22, v22, v22 row_mirror row_mask:0xf bank_mask:0xf bound_ctrl:1
	v_add_f32_dpp v21, v21, v21 row_mirror row_mask:0xf bank_mask:0xf bound_ctrl:1
	v_add_f32_dpp v20, v20, v20 row_mirror row_mask:0xf bank_mask:0xf bound_ctrl:1
	v_add_f32_dpp v19, v19, v19 row_mirror row_mask:0xf bank_mask:0xf bound_ctrl:1
	v_add_f32_dpp v18, v18, v18 row_mirror row_mask:0xf bank_mask:0xf bound_ctrl:1
	v_add_f32_dpp v2, v2, v2 row_mirror row_mask:0xf bank_mask:0xf bound_ctrl:1
	v_add_f32_dpp v3, v3, v3 row_bcast:15 row_mask:0xa bank_mask:0xf
	v_add_f32_dpp v25, v25, v25 row_bcast:15 row_mask:0xa bank_mask:0xf
	v_add_f32_dpp v24, v24, v24 row_bcast:15 row_mask:0xa bank_mask:0xf
	v_add_f32_dpp v23, v23, v23 row_bcast:15 row_mask:0xa bank_mask:0xf
	v_add_f32_dpp v22, v22, v22 row_bcast:15 row_mask:0xa bank_mask:0xf
	v_add_f32_dpp v21, v21, v21 row_bcast:15 row_mask:0xa bank_mask:0xf
	v_add_f32_dpp v20, v20, v20 row_bcast:15 row_mask:0xa bank_mask:0xf
	v_add_f32_dpp v19, v19, v19 row_bcast:15 row_mask:0xa bank_mask:0xf
	v_add_f32_dpp v18, v18, v18 row_bcast:15 row_mask:0xa bank_mask:0xf
	v_add_f32_dpp v2, v2, v2 row_bcast:15 row_mask:0xa bank_mask:0xf
	v_add_f32_dpp v3, v3, v3 row_bcast:31 row_mask:0xc bank_mask:0xf
	v_add_f32_dpp v25, v25, v25 row_bcast:31 row_mask:0xc bank_mask:0xf
	v_add_f32_dpp v24, v24, v24 row_bcast:31 row_mask:0xc bank_mask:0xf
	v_add_f32_dpp v23, v23, v23 row_bcast:31 row_mask:0xc bank_mask:0xf
	v_add_f32_dpp v22, v22, v22 row_bcast:31 row_mask:0xc bank_mask:0xf
	v_add_f32_dpp v21, v21, v21 row_bcast:31 row_mask:0xc bank_mask:0xf
	v_add_f32_dpp v20, v20, v20 row_bcast:31 row_mask:0xc bank_mask:0xf
	v_add_f32_dpp v19, v19, v19 row_bcast:31 row_mask:0xc bank_mask:0xf
	v_add_f32_dpp v18, v18, v18 row_bcast:31 row_mask:0xc bank_mask:0xf
	v_add_f32_dpp v2, v2, v2 row_bcast:31 row_mask:0xc bank_mask:0xf
	s_mov_b64 s[2:3], exec
	s_mov_b32 exec_lo, 0
	s_brev_b32 exec_hi, 1
	ds_write2_b32 v1, v3, v25 offset0:0 offset1:1
	ds_write2_b32 v1, v24, v23 offset0:2 offset1:3
	ds_write2_b32 v1, v22, v21 offset0:4 offset1:5
	ds_write2_b32 v1, v20, v19 offset0:6 offset1:7
	ds_write2_b32 v1, v18, v2 offset0:8 offset1:9
	s_mov_b64 exec, s[2:3]
	s_or_b64 exec, exec, s[2:3]
	v_cmp_gt_u32_e32 vcc, 64, v0
	s_waitcnt lgkmcnt(0)
	s_barrier
	s_and_saveexec_b64 s[2:3], vcc
	s_cbranch_execz .LBB2_111
	v_mov_b32_e32 v1, 0
	s_and_saveexec_b64 s[6:7], s[0:1]
	s_cbranch_execz .LBB2_108
	v_lshlrev_b32_e32 v1, 2, v0
	s_waitcnt vmcnt(1)
	v_add_u32_e32 v7, 0x7000, v1
	ds_read2_b32 v[2:3], v7 offset0:80 offset1:92
	ds_read2_b32 v[4:5], v7 offset0:104 offset1:116
	ds_read2_b32 v[8:9], v7 offset0:128 offset1:140
	ds_read2_b32 v[10:11], v7 offset0:152 offset1:164
	ds_read2_b32 v[12:13], v7 offset0:176 offset1:188
	s_waitcnt lgkmcnt(4)
	v_add_f32_e32 v2, 0, v2
	v_add_f32_e32 v2, v2, v3
	s_waitcnt lgkmcnt(3)
	v_add_f32_e32 v2, v2, v4
	v_add_f32_e32 v2, v2, v5
	s_waitcnt lgkmcnt(2)
	v_add_f32_e32 v2, v2, v8
	v_add_f32_e32 v2, v2, v9
	s_waitcnt lgkmcnt(1)
	v_add_f32_e32 v4, v2, v10
	ds_read2_b32 v[2:3], v7 offset0:200 offset1:212
	v_add_f32_e32 v4, v4, v11
	s_waitcnt lgkmcnt(1)
	v_add_f32_e32 v4, v4, v12
	v_add_f32_e32 v8, v4, v13
	ds_read2_b32 v[4:5], v7 offset0:224 offset1:236
	v_add_u32_e32 v1, 0x7200, v1
	s_waitcnt lgkmcnt(1)
	v_add_f32_e32 v2, v8, v2
	ds_read2_b32 v[8:9], v1 offset0:120 offset1:132
	v_add_f32_e32 v1, v2, v3
	s_waitcnt lgkmcnt(1)
	v_add_f32_e32 v1, v1, v4
	v_cvt_f32_i32_e32 v2, s14
	v_add_f32_e32 v1, v1, v5
	s_waitcnt lgkmcnt(0)
	v_add_f32_e32 v1, v1, v8
	v_add_f32_e32 v1, v1, v9
	v_div_scale_f32 v3, s[0:1], v2, v2, v1
	v_rcp_f32_e32 v4, v3
	s_mov_b32 s8, 0x42c80000
	v_fma_f32 v5, -v3, v4, 1.0
	v_fmac_f32_e32 v4, v5, v4
	v_div_scale_f32 v5, vcc, v1, v2, v1
	v_mul_f32_e32 v7, v5, v4
	v_fma_f32 v8, -v3, v7, v5
	v_fmac_f32_e32 v7, v8, v4
	v_fma_f32 v3, -v3, v7, v5
	v_div_fmas_f32 v3, v3, v4, v7
	v_div_fixup_f32 v1, v3, v2, v1
	s_waitcnt vmcnt(0)
	v_sub_f32_e32 v1, v1, v6
	v_mul_f32_e32 v2, 0.5, v1
	v_mul_f32_e32 v1, v1, v2
	v_div_scale_f32 v2, s[0:1], s8, s8, v1
	v_rcp_f32_e32 v3, v2
	s_nop 0
	v_fma_f32 v4, -v2, v3, 1.0
	v_fmac_f32_e32 v3, v4, v3
	v_div_scale_f32 v4, vcc, v1, s8, v1
	v_mul_f32_e32 v5, v4, v3
	v_fma_f32 v6, -v2, v5, v4
	v_fmac_f32_e32 v5, v6, v3
	v_fma_f32 v2, -v2, v5, v4
	v_div_fmas_f32 v2, v2, v3, v5
	v_div_fixup_f32 v1, v2, s8, v1
